# speedup vs baseline: 1.0127x; 1.0127x over previous
.LBB0_3:
	s_cmpk_gt_u32 s2, 0x7ff
	s_cbranch_scc0 .LBB0_7
	s_load_dwordx2 s[10:11], s[0:1], 0x8
	s_load_dwordx2 s[4:5], s[0:1], 0x20
	s_add_i32 s3, s2, 0xfffff800
	s_lshr_b32 s8, s3, 2
	s_and_b32 s9, s3, 3
	s_lshl_b32 s12, s8, 16
	s_lshl_b32 s13, s9, 10
	v_lshrrev_b32_e32 v1, 4, v0
	v_and_b32_e32 v2, 15, v0
	v_lshlrev_b32_e32 v3, 12, v1
	v_lshl_or_b32 v3, v2, 4, v3
	v_lshlrev_b32_e32 v4, 7, v1
	v_lshl_or_b32 v4, v2, 3, v4
	s_waitcnt lgkmcnt(0)
	s_add_u32 s10, s10, s12
	s_addc_u32 s11, s11, 0
	s_add_u32 s10, s10, s13
	s_addc_u32 s11, s11, 0
	global_load_dwordx4 v[8:11], v3, s[10:11] nt
	global_load_dwordx4 v[12:15], v3, s[10:11] offset:256 nt
	global_load_dwordx4 v[16:19], v3, s[10:11] offset:512 nt
	global_load_dwordx4 v[20:23], v3, s[10:11] offset:768 nt
	s_lshl_b32 s12, s9, 24
	s_lshl_b32 s13, s8, 11
	s_add_u32 s12, s12, s13
	s_add_u32 s4, s4, s12
	s_addc_u32 s5, s5, 0
	s_add_u32 s6, s4, 0x400000
	s_addc_u32 s7, s5, 0
	s_add_u32 s8, s4, 0x800000
	s_addc_u32 s9, s5, 0
	s_add_u32 s12, s4, 0xc00000
	s_addc_u32 s13, s5, 0
	s_mov_b32 s14, 0x4038aa3b
	s_waitcnt vmcnt(3)
	v_pk_mul_f32 v[8:9], v[8:9], s[14:15] op_sel_hi:[1,0]
	v_pk_mul_f32 v[10:11], v[10:11], s[14:15] op_sel_hi:[1,0]
	v_cvt_pk_bf16_f32 v8, v8, v9
	v_cvt_pk_bf16_f32 v9, v10, v11
	global_store_dwordx2 v4, v[8:9], s[4:5]
	s_waitcnt vmcnt(3)
	v_pk_mul_f32 v[12:13], v[12:13], s[14:15] op_sel_hi:[1,0]
	v_pk_mul_f32 v[14:15], v[14:15], s[14:15] op_sel_hi:[1,0]
	v_cvt_pk_bf16_f32 v12, v12, v13
	v_cvt_pk_bf16_f32 v13, v14, v15
	global_store_dwordx2 v4, v[12:13], s[6:7]
	s_waitcnt vmcnt(3)
	v_pk_mul_f32 v[16:17], v[16:17], s[14:15] op_sel_hi:[1,0]
	v_pk_mul_f32 v[18:19], v[18:19], s[14:15] op_sel_hi:[1,0]
	v_cvt_pk_bf16_f32 v16, v16, v17
	v_cvt_pk_bf16_f32 v17, v18, v19
	global_store_dwordx2 v4, v[16:17], s[8:9]
	s_waitcnt vmcnt(3)
	v_pk_mul_f32 v[20:21], v[20:21], s[14:15] op_sel_hi:[1,0]
	v_pk_mul_f32 v[22:23], v[22:23], s[14:15] op_sel_hi:[1,0]
	v_cvt_pk_bf16_f32 v20, v20, v21
	v_cvt_pk_bf16_f32 v21, v22, v23
	global_store_dwordx2 v4, v[20:21], s[12:13]
	s_endpgm

	.amdhsa_kernel _Z6prep_kPKfS0_S0_PDF16_S1_S1_S1_S1_S0_Pf
		.amdhsa_group_segment_fixed_size 8448
		.amdhsa_private_segment_fixed_size 0
		.amdhsa_kernarg_size 80
		.amdhsa_user_sgpr_count 2
		.amdhsa_user_sgpr_dispatch_ptr 0
		.amdhsa_user_sgpr_queue_ptr 0
		.amdhsa_user_sgpr_kernarg_segment_ptr 1
		.amdhsa_user_sgpr_dispatch_id 0
		.amdhsa_user_sgpr_kernarg_preload_length 0
		.amdhsa_user_sgpr_kernarg_preload_offset 0
		.amdhsa_user_sgpr_private_segment_size 0
		.amdhsa_uses_dynamic_stack 0
		.amdhsa_enable_private_segment 0
		.amdhsa_system_sgpr_workgroup_id_x 1
		.amdhsa_system_sgpr_workgroup_id_y 0
		.amdhsa_system_sgpr_workgroup_id_z 0
		.amdhsa_system_sgpr_workgroup_info 0
		.amdhsa_system_vgpr_workitem_id 0
		.amdhsa_next_free_vgpr 34
		.amdhsa_next_free_sgpr 16
		.amdhsa_accum_offset 36
		.amdhsa_reserve_vcc 1
		.amdhsa_float_round_mode_32 0
		.amdhsa_float_round_mode_16_64 0
		.amdhsa_float_denorm_mode_32 3
		.amdhsa_float_denorm_mode_16_64 3
		.amdhsa_dx10_clamp 1
		.amdhsa_ieee_mode 1
		.amdhsa_fp16_overflow 0
		.amdhsa_tg_split 0
		.amdhsa_exception_fp_ieee_invalid_op 0
		.amdhsa_exception_fp_denorm_src 0
		.amdhsa_exception_fp_ieee_div_zero 0
		.amdhsa_exception_fp_ieee_overflow 0
		.amdhsa_exception_fp_ieee_underflow 0
		.amdhsa_exception_fp_ieee_inexact 0
		.amdhsa_exception_int_div_zero 0
	.end_amdhsa_kernel

_Z6gemm_kILi2EEvPKDF16_S1_iiiiPfPDF16_PKfS2_:
	s_lshl_b32 s3, s2, 3
	s_load_dwordx2 s[46:47], s[0:1], 0x30
	s_load_dwordx2 s[4:5], s[0:1], 0x8
	s_load_dwordx2 s[8:9], s[0:1], 0x0
	s_load_dwordx2 s[14:15], s[0:1], 0x28
	s_and_b32 s18, s3, 56
	s_ashr_i32 s3, s2, 5
	s_add_i32 s18, s18, s3
	s_lshl_b32 s6, s18, 8
	s_and_b32 s13, s6, 0xf00
	s_ashr_i32 s12, s18, 4
	v_lshrrev_b32_e32 v132, 8, v0
	v_readfirstlane_b32 s3, v0
	s_mul_i32 s16, s12, 0x84
	s_ashr_i32 s17, s16, 31
	s_lshl_b64 s[48:49], s[16:17], 19
	s_add_i32 s20, 0, 0x20000
	s_mov_b32 s7, 0x20000
	s_brev_b32 s6, -2
	s_movk_i32 s50, 0x100
	s_waitcnt lgkmcnt(0)
	v_cmp_gt_u32_e64 s[0:1], s50, v0
	s_add_u32 s4, s4, s48
	s_addc_u32 s48, s5, s49
	s_and_b32 s5, s48, 0xffff
	s_lshl_b32 s50, s13, 2
	s_add_u32 s46, s46, s50
	s_addc_u32 s47, s47, 0
	v_lshrrev_b32_e32 v1, 3, v0
	v_lshlrev_b32_e32 v2, 4, v0
	v_xor_b32_e32 v1, v1, v0
	v_and_b32_e32 v4, 0x1f80, v2
	v_lshlrev_b32_e32 v5, 4, v1
	s_movk_i32 s18, 0x70
	v_lshlrev_b32_e32 v6, 2, v0
	v_lshlrev_b32_e32 v3, 3, v1
	v_and_or_b32 v1, v5, s18, v4
	v_lshlrev_b32_e32 v4, 3, v0
	v_and_b32_e32 v6, 32, v6
	s_movk_i32 s19, 0xf80
	v_and_b32_e32 v5, 64, v5
	v_and_b32_e32 v3, 24, v3
	v_and_or_b32 v4, v4, s19, v6
	v_or3_b32 v3, v4, v5, v3
	v_lshlrev_b32_e32 v130, 1, v3
	v_or_b32_e32 v3, 0x2000, v2
	s_lshl_b32 s10, s2, 5
	v_lshrrev_b32_e32 v4, 7, v3
	s_and_b32 s21, s10, 0x300
	s_lshl_b32 s3, s3, 4
	s_lshl_b64 s[10:11], s[16:17], 17
	v_xor_b32_e32 v4, v4, v0
	s_movk_i32 s19, 0x3f80
	v_mov_b32_e32 v7, 0x2000
	v_lshlrev_b32_e32 v5, 3, v4
	v_bitop3_b32 v2, v2, s19, v7 bitop3:0xc8
	v_lshlrev_b32_e32 v4, 4, v4
	s_movk_i32 s17, 0x1f80
	v_and_or_b32 v131, v4, s18, v2
	v_lshrrev_b32_e32 v2, 1, v3
	s_add_i32 s3, s3, 0
	v_and_b32_e32 v3, 64, v4
	v_and_b32_e32 v4, 24, v5
	v_and_or_b32 v2, v2, s17, v6
	s_add_i32 s17, s3, 0x10000
	v_or3_b32 v2, v2, v3, v4
	s_lshl_b32 s18, s13, 7
	s_mov_b32 m0, s17
	s_add_i32 s22, s3, 0x12000
	s_lshl_b32 s23, s13, 6
	v_lshlrev_b32_e32 v133, 1, v2
	buffer_load_dwordx4 v130, s[4:7], s18 offen lds
	s_mov_b32 m0, s22
	s_or_b32 s24, s23, 0x2000
	s_add_i32 s25, s3, 0x14000
	buffer_load_dwordx4 v133, s[4:7], s18 offen lds
	s_lshl_b32 s19, s24, 1
	s_mov_b32 m0, s25
	s_add_i32 s26, s3, 0x16000
	buffer_load_dwordx4 v130, s[4:7], s19 offen lds
	s_mov_b32 m0, s26
	s_and_b32 s9, s9, 0xffff
	s_mov_b32 s11, 0x20000
	s_brev_b32 s10, -2
	buffer_load_dwordx4 v133, s[4:7], s19 offen lds
	s_lshl_b32 s28, s21, 7
	s_mov_b32 m0, s3
	s_add_i32 s27, s3, 0x2000
	v_lshrrev_b32_e32 v140, 3, v0
	v_and_b32_e32 v141, 7, v0
	v_bfe_u32 v142, v140, 1, 1
	v_bfe_u32 v143, v140, 3, 1
	v_lshl_or_b32 v142, v143, 1, v142
	v_lshrrev_b32_e32 v143, 1, v141
	v_xor_b32_e32 v142, v142, v143
	v_and_b32_e32 v141, 1, v141
	v_lshlrev_b32_e32 v140, 7, v140
	v_lshl_or_b32 v140, v142, 5, v140
	v_lshl_or_b32 v1, v141, 4, v140
	v_mov_b32_e32 v131, v1
	s_lshl_b32 s54, s21, 11
	s_lshl_b32 s55, s21, 16
	s_add_i32 s55, s55, 0x41e0000
	s_mov_b32 s63, 0x400000
	s_mov_b32 s60, s16
	s_cmp_lt_u32 s60, 16
	s_cselect_b32 s61, s54, s55
	s_cselect_b32 s62, 0x20000, s63
	s_lshl_b32 s60, s60, 13
	s_add_i32 s56, s61, s60
	s_add_i32 s57, s56, s62
	s_add_i32 s58, s57, s62
	s_add_i32 s59, s58, s62
	buffer_load_dwordx4 v1, s[8:11], s56 offen lds
	s_mov_b32 m0, s27
	s_add_i32 s30, s3, 0x4000
	buffer_load_dwordx4 v1, s[8:11], s57 offen lds
	s_lshl_b32 s28, s21, 6
	s_or_b32 s29, s28, 0x2000
	s_lshl_b32 s33, s29, 1
	s_mov_b32 m0, s30
	s_add_i32 s31, s3, 0x6000
	buffer_load_dwordx4 v1, s[8:11], s58 offen lds
	s_mov_b32 m0, s31
	s_bitset1_b32 s18, 19
	buffer_load_dwordx4 v1, s[8:11], s59 offen lds
	s_add_i32 s33, s3, 0x18000
	s_mov_b32 m0, s33
	s_add_i32 s34, s3, 0x1a000
	buffer_load_dwordx4 v130, s[4:7], s18 offen lds
	s_mov_b32 m0, s34
	s_add_i32 s35, s3, 0x1c000
	buffer_load_dwordx4 v133, s[4:7], s18 offen lds
	s_bitset1_b32 s19, 19
	s_mov_b32 m0, s35
	s_add_i32 s36, s3, 0x1e000
	buffer_load_dwordx4 v130, s[4:7], s19 offen lds
	s_mov_b32 m0, s36
	s_mov_b32 s37, 2
	buffer_load_dwordx4 v133, s[4:7], s19 offen lds
	v_and_b32_e32 v221, 0xff, v0
	v_lshlrev_b32_e32 v220, 2, v221
	s_lshr_b32 s50, s3, 12
	s_lshl_b32 s50, s50, 4
	s_lshl_b32 s51, s12, 6
	s_add_i32 s50, s50, s51
	s_lshl_b32 s50, s50, 14
	s_add_u32 s46, s46, s50
	s_addc_u32 s47, s47, 0
	global_load_dword v10, v220, s[46:47]
	s_add_u32 s46, s46, 0x4000
	s_addc_u32 s47, s47, 0
	global_load_dword v11, v220, s[46:47]
	s_add_u32 s46, s46, 0x4000
	s_addc_u32 s47, s47, 0
	global_load_dword v12, v220, s[46:47]
	s_add_u32 s46, s46, 0x4000
	s_addc_u32 s47, s47, 0
	global_load_dword v13, v220, s[46:47]
	s_add_u32 s46, s46, 0x4000
	s_addc_u32 s47, s47, 0
	global_load_dword v14, v220, s[46:47]
	s_add_u32 s46, s46, 0x4000
	s_addc_u32 s47, s47, 0
	global_load_dword v15, v220, s[46:47]
	s_add_u32 s46, s46, 0x4000
	s_addc_u32 s47, s47, 0
	global_load_dword v16, v220, s[46:47]
	s_add_u32 s46, s46, 0x4000
	s_addc_u32 s47, s47, 0
	global_load_dword v17, v220, s[46:47]
	s_add_u32 s46, s46, 0x4000
	s_addc_u32 s47, s47, 0
	global_load_dword v18, v220, s[46:47]
	s_add_u32 s46, s46, 0x4000
	s_addc_u32 s47, s47, 0
	global_load_dword v19, v220, s[46:47]
	s_add_u32 s46, s46, 0x4000
	s_addc_u32 s47, s47, 0
	global_load_dword v20, v220, s[46:47]
	s_add_u32 s46, s46, 0x4000
	s_addc_u32 s47, s47, 0
	global_load_dword v21, v220, s[46:47]
	s_add_u32 s46, s46, 0x4000
	s_addc_u32 s47, s47, 0
	global_load_dword v22, v220, s[46:47]
	s_add_u32 s46, s46, 0x4000
	s_addc_u32 s47, s47, 0
	global_load_dword v23, v220, s[46:47]
	s_add_u32 s46, s46, 0x4000
	s_addc_u32 s47, s47, 0
	global_load_dword v24, v220, s[46:47]
	s_add_u32 s46, s46, 0x4000
	s_addc_u32 s47, s47, 0
	global_load_dword v25, v220, s[46:47]
	s_add_u32 s46, s46, 0x44000
	s_addc_u32 s47, s47, 0
	global_load_dword v26, v220, s[46:47]
	s_add_u32 s46, s46, 0x4000
	s_addc_u32 s47, s47, 0
	global_load_dword v27, v220, s[46:47]
	s_add_u32 s46, s46, 0x4000
	s_addc_u32 s47, s47, 0
	global_load_dword v28, v220, s[46:47]
	s_add_u32 s46, s46, 0x4000
	s_addc_u32 s47, s47, 0
	global_load_dword v29, v220, s[46:47]
	s_add_u32 s46, s46, 0x4000
	s_addc_u32 s47, s47, 0
	global_load_dword v30, v220, s[46:47]
	s_add_u32 s46, s46, 0x4000
	s_addc_u32 s47, s47, 0
	global_load_dword v31, v220, s[46:47]
	s_add_u32 s46, s46, 0x4000
	s_addc_u32 s47, s47, 0
	global_load_dword v32, v220, s[46:47]
	s_add_u32 s46, s46, 0x4000
	s_addc_u32 s47, s47, 0
	global_load_dword v33, v220, s[46:47]
	s_add_u32 s46, s46, 0x4000
	s_addc_u32 s47, s47, 0
	global_load_dword v34, v220, s[46:47]
	s_add_u32 s46, s46, 0x4000
	s_addc_u32 s47, s47, 0
	global_load_dword v35, v220, s[46:47]
	s_add_u32 s46, s46, 0x4000
	s_addc_u32 s47, s47, 0
	global_load_dword v36, v220, s[46:47]
	s_add_u32 s46, s46, 0x4000
	s_addc_u32 s47, s47, 0
	global_load_dword v37, v220, s[46:47]
	s_add_u32 s46, s46, 0x4000
	s_addc_u32 s47, s47, 0
	global_load_dword v38, v220, s[46:47]
	s_add_u32 s46, s46, 0x4000
	s_addc_u32 s47, s47, 0
	global_load_dword v39, v220, s[46:47]
	s_add_u32 s46, s46, 0x4000
	s_addc_u32 s47, s47, 0
	global_load_dword v40, v220, s[46:47]
	s_add_u32 s46, s46, 0x4000
	s_addc_u32 s47, s47, 0
	global_load_dword v41, v220, s[46:47]
	v_mov_b32_e32 v8, 0
	s_cmp_lt_i32 s12, 1
	s_cbranch_scc1 .Lg2_skip0
	s_sub_u32 s46, s46, 0x13c000
	s_subb_u32 s47, s47, 0
	global_load_dword v42, v220, s[46:47]
	s_add_u32 s46, s46, 0x4000
	s_addc_u32 s47, s47, 0
	global_load_dword v43, v220, s[46:47]
	s_add_u32 s46, s46, 0x4000
	s_addc_u32 s47, s47, 0
	global_load_dword v44, v220, s[46:47]
	s_add_u32 s46, s46, 0x4000
	s_addc_u32 s47, s47, 0
	global_load_dword v45, v220, s[46:47]
	s_add_u32 s46, s46, 0x4000
	s_addc_u32 s47, s47, 0
	global_load_dword v46, v220, s[46:47]
	s_add_u32 s46, s46, 0x4000
	s_addc_u32 s47, s47, 0
	global_load_dword v47, v220, s[46:47]
	s_add_u32 s46, s46, 0x4000
	s_addc_u32 s47, s47, 0
	global_load_dword v48, v220, s[46:47]
	s_add_u32 s46, s46, 0x4000
	s_addc_u32 s47, s47, 0
	global_load_dword v49, v220, s[46:47]
	s_add_u32 s46, s46, 0x4000
	s_addc_u32 s47, s47, 0
	global_load_dword v50, v220, s[46:47]
	s_add_u32 s46, s46, 0x4000
	s_addc_u32 s47, s47, 0
	global_load_dword v51, v220, s[46:47]
	s_add_u32 s46, s46, 0x4000
	s_addc_u32 s47, s47, 0
	global_load_dword v52, v220, s[46:47]
	s_add_u32 s46, s46, 0x4000
	s_addc_u32 s47, s47, 0
	global_load_dword v53, v220, s[46:47]
	s_add_u32 s46, s46, 0x4000
	s_addc_u32 s47, s47, 0
	global_load_dword v54, v220, s[46:47]
	s_add_u32 s46, s46, 0x4000
	s_addc_u32 s47, s47, 0
	global_load_dword v55, v220, s[46:47]
	s_add_u32 s46, s46, 0x4000
	s_addc_u32 s47, s47, 0
	global_load_dword v56, v220, s[46:47]
	s_add_u32 s46, s46, 0x4000
	s_addc_u32 s47, s47, 0
	global_load_dword v57, v220, s[46:47]

.Lg2_skip0b:
	v_mul_u32_u24_e32 v5, 0xc00, v132
	v_add3_u32 v2, s20, v5, v220
	ds_write2st64_b32 v2, v8, v3 offset0:12 offset1:16
	ds_write_b32 v2, v4 offset:5120
	s_waitcnt lgkmcnt(0)
	s_barrier
	s_and_saveexec_b64 s[50:51], s[0:1]
	s_cbranch_execz .Lg2_ratio_done
	s_cmp_eq_u32 s12, 0
	v_mov_b32_e32 v2, 0x4038aa3b
	s_cbranch_scc1 .LBB4_10
	v_lshl_add_u32 v2, v221, 2, s20
	v_lshl_add_u32 v3, v0, 2, s20
	ds_read_b32 v3, v3 offset:3072
	ds_read_b32 v2, v2 offset:6144
	s_waitcnt lgkmcnt(0)
	v_add_f32_e32 v2, v3, v2

.LBB4_13:
	s_or_b64 exec, exec, s[18:19]
	v_and_b32_e32 v135, 15, v0
	v_bfe_u32 v136, v0, 6, 2
	v_lshlrev_b32_e32 v5, 12, v136
	v_lshlrev_b32_e32 v6, 7, v135
	s_add_i32 s38, 0, 0x10000
	s_add_i32 s40, 0, 0x18000
	v_lshrrev_b32_e32 v134, 4, v0
	v_bfe_u32 v2, v0, 4, 2
	v_and_b32_e32 v3, 7, v0
	v_add3_u32 v7, s38, v5, v6
	s_add_i32 s38, 0, 0x10800
	v_add3_u32 v11, s40, v5, v6
	s_add_i32 s40, 0, 0x18800
	v_bitop3_b32 v4, v134, v3, 3 bitop3:0x6c
	v_bitop3_b32 v2, v2, v3, 4 bitop3:0x36
	v_add3_u32 v3, s38, v5, v6
	s_add_i32 s38, 0, 0x14000
	v_add3_u32 v12, s40, v5, v6
	s_add_i32 s40, 0, 0x1c000
	v_add3_u32 v8, s38, v5, v6
	s_add_i32 s38, 0, 0x14800
	v_add3_u32 v13, s40, v5, v6
	s_add_i32 s40, 0, 0x1c800
	v_add3_u32 v9, s38, v5, v6
	v_lshlrev_b32_e32 v10, 13, v132
	v_add3_u32 v5, s40, v5, v6
	s_lshl_b32 s40, s12, 6
	v_add3_u32 v10, 0, v10, v6
	v_lshl_add_u32 v6, v136, 7, s40
	v_lshl_or_b32 v6, v135, 2, v6
	v_mov_b32_e32 v26, 0
	s_waitcnt vmcnt(4)
	v_lshlrev_b32_e32 v4, 4, v4
	v_lshlrev_b32_e32 v2, 4, v2
	v_add_u32_e32 v6, 0, v6
	s_lshl_b32 s2, s2, 12
	v_mov_b32_e32 v27, v26
	v_mov_b32_e32 v28, v26
	v_mov_b32_e32 v29, v26
	v_add_u32_e32 v137, 0x1ff20, v6
	s_and_b32 s2, s2, 0x18000
	v_add_u32_e32 v138, v7, v4
	v_add_u32_e32 v139, v7, v2
	v_add_u32_e32 v140, v3, v4
	v_add_u32_e32 v141, v3, v2
	v_add_u32_e32 v142, v8, v4
	v_add_u32_e32 v143, v8, v2
	v_add_u32_e32 v144, v9, v4
	v_add_u32_e32 v145, v9, v2
	v_add_u32_e32 v146, v10, v4
	v_add_u32_e32 v147, v10, v2
	v_and_b32_e32 v156, 15, v0
	v_bfe_u32 v157, v0, 4, 2
	v_lshlrev_b32_e32 v158, 13, v132
	v_lshl_or_b32 v158, v157, 10, v158
	v_lshrrev_b32_e32 v159, 2, v156
	v_lshl_or_b32 v158, v159, 7, v158
	v_and_b32_e32 v159, 3, v156
	v_lshl_or_b32 v158, v159, 3, v158
	v_lshrrev_b32_e32 v159, 3, v156
	v_and_b32_e32 v160, 1, v157
	v_lshl_or_b32 v160, v160, 1, v159
	v_xor_b32_e32 v161, 0, v160
	v_lshl_or_b32 v146, v161, 5, v158
	v_xor_b32_e32 v161, 1, v160
	v_lshl_or_b32 v147, v161, 5, v158
	v_xor_b32_e32 v161, 2, v160
	v_lshl_or_b32 v222, v161, 5, v158
	v_xor_b32_e32 v161, 3, v160
	v_lshl_or_b32 v223, v161, 5, v158
	v_add_u32_e32 v148, v11, v4
	v_add_u32_e32 v149, v11, v2
	v_add_u32_e32 v150, v12, v4
	v_add_u32_e32 v151, v12, v2
	v_add_u32_e32 v152, v13, v4
	v_add_u32_e32 v153, v13, v2
	v_add_u32_e32 v154, v5, v4
	v_add_u32_e32 v155, v5, v2
	v_mov_b64_e32 v[2:3], v[26:27]
	v_mov_b64_e32 v[40:41], v[28:29]
	v_mov_b64_e32 v[10:11], v[26:27]
	v_mov_b64_e32 v[48:49], v[28:29]
	v_mov_b64_e32 v[68:69], v[28:29]
	v_mov_b64_e32 v[100:101], v[28:29]
	v_mov_b64_e32 v[72:73], v[28:29]
	v_mov_b64_e32 v[104:105], v[28:29]
	v_mov_b64_e32 v[76:77], v[28:29]
	v_mov_b64_e32 v[108:109], v[28:29]
	v_mov_b64_e32 v[80:81], v[28:29]
	v_mov_b64_e32 v[112:113], v[28:29]
	v_mov_b64_e32 v[18:19], v[26:27]
	v_mov_b64_e32 v[52:53], v[28:29]
	v_mov_b64_e32 v[22:23], v[26:27]
	v_mov_b64_e32 v[56:57], v[28:29]
	v_mov_b64_e32 v[32:33], v[28:29]
	v_mov_b64_e32 v[60:61], v[28:29]
	v_mov_b64_e32 v[36:37], v[28:29]
	v_mov_b64_e32 v[64:65], v[28:29]
	v_mov_b64_e32 v[84:85], v[28:29]
	v_mov_b64_e32 v[116:117], v[28:29]
	v_mov_b64_e32 v[88:89], v[28:29]
	v_mov_b64_e32 v[120:121], v[28:29]
	v_mov_b64_e32 v[92:93], v[28:29]
	v_mov_b64_e32 v[124:125], v[28:29]
	v_mov_b64_e32 v[96:97], v[28:29]
	v_mov_b64_e32 v[128:129], v[28:29]
	v_mov_b64_e32 v[14:15], v[26:27]
	v_mov_b64_e32 v[44:45], v[28:29]
	v_mov_b64_e32 v[6:7], v[26:27]
	s_add_i32 s18, s3, 0x8000
	s_add_i32 s19, s3, 0xc000
	s_add_i32 s38, s3, 0xa000
	s_add_i32 s39, s3, 0xe000
	s_or_b32 s2, s2, 0x24000
	v_mov_b64_e32 v[4:5], v[28:29]
	v_mov_b64_e32 v[38:39], v[26:27]
	v_mov_b64_e32 v[12:13], v[28:29]
	v_mov_b64_e32 v[46:47], v[26:27]
	v_mov_b64_e32 v[66:67], v[26:27]
	v_mov_b64_e32 v[98:99], v[26:27]
	v_mov_b64_e32 v[70:71], v[26:27]
	v_mov_b64_e32 v[102:103], v[26:27]
	v_mov_b64_e32 v[74:75], v[26:27]
	v_mov_b64_e32 v[106:107], v[26:27]
	v_mov_b64_e32 v[78:79], v[26:27]
	v_mov_b64_e32 v[110:111], v[26:27]
	v_mov_b64_e32 v[20:21], v[28:29]
	v_mov_b64_e32 v[50:51], v[26:27]
	v_mov_b64_e32 v[24:25], v[28:29]
	v_mov_b64_e32 v[54:55], v[26:27]
	v_mov_b64_e32 v[30:31], v[26:27]
	v_mov_b64_e32 v[58:59], v[26:27]
	v_mov_b64_e32 v[34:35], v[26:27]
	v_mov_b64_e32 v[62:63], v[26:27]
	v_mov_b64_e32 v[82:83], v[26:27]
	v_mov_b64_e32 v[114:115], v[26:27]
	v_mov_b64_e32 v[86:87], v[26:27]
	v_mov_b64_e32 v[118:119], v[26:27]
	v_mov_b64_e32 v[90:91], v[26:27]
	v_mov_b64_e32 v[122:123], v[26:27]
	v_mov_b64_e32 v[94:95], v[26:27]
	v_mov_b64_e32 v[126:127], v[26:27]
	v_mov_b64_e32 v[16:17], v[28:29]
	v_mov_b64_e32 v[42:43], v[26:27]
	v_mov_b64_e32 v[8:9], v[28:29]
	s_barrier
	s_barrier
	s_branch .LBB4_15

.LBB4_15:
	ds_read_b128 v[156:159], v138
	ds_read_b128 v[160:163], v139
	ds_read_b128 v[164:167], v140
	ds_read_b128 v[168:171], v141
	ds_read_b128 v[172:175], v142
	ds_read_b128 v[176:179], v143
	ds_read_b128 v[180:183], v144
	ds_read_b128 v[184:187], v145
	s_add_i32 s40, s37, -2
	s_min_u32 s41, s37, 0x83
	s_add_i32 s42, s2, 0xffffc000
	s_mov_b32 m0, s18
	ds_read_b64_tr_b16 v[188:189], v146
	ds_read_b64_tr_b16 v[190:191], v146 offset:512
	ds_read_b64_tr_b16 v[192:193], v147
	ds_read_b64_tr_b16 v[194:195], v147 offset:512
	ds_read_b64_tr_b16 v[196:197], v146 offset:4096
	ds_read_b64_tr_b16 v[198:199], v146 offset:4608
	ds_read_b64_tr_b16 v[200:201], v147 offset:4096
	ds_read_b64_tr_b16 v[202:203], v147 offset:4608
	ds_read_b64_tr_b16 v[204:205], v222
	ds_read_b64_tr_b16 v[206:207], v222 offset:512
	ds_read_b64_tr_b16 v[208:209], v223
	ds_read_b64_tr_b16 v[210:211], v223 offset:512
	ds_read_b64_tr_b16 v[212:213], v222 offset:4096
	ds_read_b64_tr_b16 v[214:215], v222 offset:4608
	ds_read_b64_tr_b16 v[216:217], v223 offset:4096
	ds_read_b64_tr_b16 v[218:219], v223 offset:4608
	s_add_i32 s60, s16, s37
	s_add_i32 s60, s60, -1
	s_cmp_lt_u32 s60, 16
	s_cselect_b32 s61, s54, s55
	s_cselect_b32 s62, 0x20000, s63
	s_lshl_b32 s60, s60, 13
	s_add_i32 s56, s61, s60
	s_add_i32 s57, s56, s62
	s_add_i32 s58, s57, s62
	s_add_i32 s59, s58, s62
	buffer_load_dwordx4 v1, s[8:11], s56 offen lds
	s_mov_b32 m0, s38
	s_nop 0
	buffer_load_dwordx4 v1, s[8:11], s57 offen lds
	s_mov_b32 m0, s19
	s_nop 0
	buffer_load_dwordx4 v1, s[8:11], s58 offen lds
	s_mov_b32 m0, s39
	s_nop 0
	buffer_load_dwordx4 v1, s[8:11], s59 offen lds
	s_waitcnt lgkmcnt(15)
	s_barrier
	s_waitcnt lgkmcnt(0)
	s_setprio 1
	s_waitcnt lgkmcnt(7)
	v_mfma_f32_16x16x32_bf16 v[126:129], v[188:191], v[156:159], v[126:129]
	v_mfma_f32_16x16x32_bf16 v[94:97], v[188:191], v[164:167], v[94:97]
	s_waitcnt lgkmcnt(6)
	v_mfma_f32_16x16x32_bf16 v[122:125], v[192:195], v[156:159], v[122:125]
	v_mfma_f32_16x16x32_bf16 v[90:93], v[192:195], v[164:167], v[90:93]
	s_waitcnt lgkmcnt(3)
	v_mfma_f32_16x16x32_bf16 v[118:121], v[204:207], v[156:159], v[118:121]
	v_mfma_f32_16x16x32_bf16 v[86:89], v[204:207], v[164:167], v[86:89]
	s_waitcnt lgkmcnt(2)
	v_mfma_f32_16x16x32_bf16 v[114:117], v[208:211], v[156:159], v[114:117]
	v_mfma_f32_16x16x32_bf16 v[82:85], v[208:211], v[164:167], v[82:85]
	v_mfma_f32_16x16x32_bf16 v[126:129], v[196:199], v[160:163], v[126:129]
	v_mfma_f32_16x16x32_bf16 v[94:97], v[196:199], v[168:171], v[94:97]
	v_mfma_f32_16x16x32_bf16 v[122:125], v[200:203], v[160:163], v[122:125]
	v_mfma_f32_16x16x32_bf16 v[90:93], v[200:203], v[168:171], v[90:93]
	s_waitcnt lgkmcnt(1)
	v_mfma_f32_16x16x32_bf16 v[118:121], v[212:215], v[160:163], v[118:121]
	v_mfma_f32_16x16x32_bf16 v[86:89], v[212:215], v[168:171], v[86:89]
	s_waitcnt lgkmcnt(0)
	v_mfma_f32_16x16x32_bf16 v[114:117], v[216:219], v[160:163], v[114:117]
	v_mfma_f32_16x16x32_bf16 v[82:85], v[216:219], v[168:171], v[82:85]
	s_setprio 0
	s_setprio 1
	v_mfma_f32_16x16x32_bf16 v[62:65], v[188:191], v[172:175], v[62:65]
	v_mfma_f32_16x16x32_bf16 v[34:37], v[188:191], v[180:183], v[34:37]
	v_mfma_f32_16x16x32_bf16 v[58:61], v[192:195], v[172:175], v[58:61]
	v_mfma_f32_16x16x32_bf16 v[30:33], v[192:195], v[180:183], v[30:33]
	v_mfma_f32_16x16x32_bf16 v[54:57], v[204:207], v[172:175], v[54:57]
	v_mfma_f32_16x16x32_bf16 v[22:25], v[204:207], v[180:183], v[22:25]
	v_mfma_f32_16x16x32_bf16 v[50:53], v[208:211], v[172:175], v[50:53]
	v_mfma_f32_16x16x32_bf16 v[18:21], v[208:211], v[180:183], v[18:21]
	v_mfma_f32_16x16x32_bf16 v[62:65], v[196:199], v[176:179], v[62:65]
	v_mfma_f32_16x16x32_bf16 v[34:37], v[196:199], v[184:187], v[34:37]
	v_mfma_f32_16x16x32_bf16 v[58:61], v[200:203], v[176:179], v[58:61]
	v_mfma_f32_16x16x32_bf16 v[30:33], v[200:203], v[184:187], v[30:33]
	v_mfma_f32_16x16x32_bf16 v[54:57], v[212:215], v[176:179], v[54:57]
	v_mfma_f32_16x16x32_bf16 v[22:25], v[212:215], v[184:187], v[22:25]
	v_mfma_f32_16x16x32_bf16 v[50:53], v[216:219], v[176:179], v[50:53]
	v_mfma_f32_16x16x32_bf16 v[18:21], v[216:219], v[184:187], v[18:21]
	s_setprio 0
	s_barrier
	s_lshl_b32 s42, s41, 18
	s_or_b32 s43, s42, s23
	s_mov_b32 m0, s17
	s_lshl_b32 s43, s43, 1
	ds_read_b64_tr_b16 v[188:189], v146 offset:16384
	ds_read_b64_tr_b16 v[190:191], v146 offset:16896
	ds_read_b64_tr_b16 v[192:193], v147 offset:16384
	ds_read_b64_tr_b16 v[194:195], v147 offset:16896
	ds_read_b64_tr_b16 v[196:197], v146 offset:20480
	ds_read_b64_tr_b16 v[198:199], v146 offset:20992
	ds_read_b64_tr_b16 v[200:201], v147 offset:20480
	ds_read_b64_tr_b16 v[202:203], v147 offset:20992
	ds_read_b64_tr_b16 v[204:205], v222 offset:16384
	ds_read_b64_tr_b16 v[206:207], v222 offset:16896
	ds_read_b64_tr_b16 v[208:209], v223 offset:16384
	ds_read_b64_tr_b16 v[210:211], v223 offset:16896
	ds_read_b64_tr_b16 v[212:213], v222 offset:20480
	ds_read_b64_tr_b16 v[214:215], v222 offset:20992
	ds_read_b64_tr_b16 v[216:217], v223 offset:20480
	ds_read_b64_tr_b16 v[218:219], v223 offset:20992
	buffer_load_dwordx4 v130, s[4:7], s43 offen lds
	s_mov_b32 m0, s22
	s_or_b32 s42, s42, s24
	buffer_load_dwordx4 v133, s[4:7], s43 offen lds
	s_lshl_b32 s42, s42, 1
	s_mov_b32 m0, s25
	s_nop 0
	buffer_load_dwordx4 v130, s[4:7], s42 offen lds
	s_mov_b32 m0, s26
	s_nop 0
	buffer_load_dwordx4 v133, s[4:7], s42 offen lds
	s_waitcnt lgkmcnt(0)
	s_waitcnt vmcnt(4)
	s_barrier
	s_setprio 1
	s_waitcnt lgkmcnt(7)
	v_mfma_f32_16x16x32_bf16 v[110:113], v[188:191], v[156:159], v[110:113]
	v_mfma_f32_16x16x32_bf16 v[78:81], v[188:191], v[164:167], v[78:81]
	s_waitcnt lgkmcnt(6)
	v_mfma_f32_16x16x32_bf16 v[106:109], v[192:195], v[156:159], v[106:109]
	v_mfma_f32_16x16x32_bf16 v[74:77], v[192:195], v[164:167], v[74:77]
	s_waitcnt lgkmcnt(3)
	v_mfma_f32_16x16x32_bf16 v[102:105], v[204:207], v[156:159], v[102:105]
	v_mfma_f32_16x16x32_bf16 v[70:73], v[204:207], v[164:167], v[70:73]
	s_waitcnt lgkmcnt(2)
	v_mfma_f32_16x16x32_bf16 v[98:101], v[208:211], v[156:159], v[98:101]
	v_mfma_f32_16x16x32_bf16 v[66:69], v[208:211], v[164:167], v[66:69]
	v_mfma_f32_16x16x32_bf16 v[110:113], v[196:199], v[160:163], v[110:113]
	v_mfma_f32_16x16x32_bf16 v[78:81], v[196:199], v[168:171], v[78:81]
	v_mfma_f32_16x16x32_bf16 v[106:109], v[200:203], v[160:163], v[106:109]
	v_mfma_f32_16x16x32_bf16 v[74:77], v[200:203], v[168:171], v[74:77]
	s_waitcnt lgkmcnt(1)
	v_mfma_f32_16x16x32_bf16 v[102:105], v[212:215], v[160:163], v[102:105]
	v_mfma_f32_16x16x32_bf16 v[70:73], v[212:215], v[168:171], v[70:73]
	s_waitcnt lgkmcnt(0)
	v_mfma_f32_16x16x32_bf16 v[98:101], v[216:219], v[160:163], v[98:101]
	v_mfma_f32_16x16x32_bf16 v[66:69], v[216:219], v[168:171], v[66:69]
	s_setprio 0
	s_setprio 1
	v_mfma_f32_16x16x32_bf16 v[46:49], v[188:191], v[172:175], v[46:49]
	v_mfma_f32_16x16x32_bf16 v[10:13], v[188:191], v[180:183], v[10:13]
	v_mfma_f32_16x16x32_bf16 v[38:41], v[192:195], v[172:175], v[38:41]
	v_mfma_f32_16x16x32_bf16 v[2:5], v[192:195], v[180:183], v[2:5]
	v_mfma_f32_16x16x32_bf16 v[26:29], v[204:207], v[172:175], v[26:29]
	v_mfma_f32_16x16x32_bf16 v[14:17], v[204:207], v[180:183], v[14:17]
	v_mfma_f32_16x16x32_bf16 v[42:45], v[208:211], v[172:175], v[42:45]
	v_mfma_f32_16x16x32_bf16 v[6:9], v[208:211], v[180:183], v[6:9]
	v_mfma_f32_16x16x32_bf16 v[46:49], v[196:199], v[176:179], v[46:49]
	v_mfma_f32_16x16x32_bf16 v[10:13], v[196:199], v[184:187], v[10:13]
	v_mfma_f32_16x16x32_bf16 v[38:41], v[200:203], v[176:179], v[38:41]
	v_mfma_f32_16x16x32_bf16 v[2:5], v[200:203], v[184:187], v[2:5]
	v_mfma_f32_16x16x32_bf16 v[26:29], v[212:215], v[176:179], v[26:29]
	v_mfma_f32_16x16x32_bf16 v[14:17], v[212:215], v[184:187], v[14:17]
	v_mfma_f32_16x16x32_bf16 v[42:45], v[216:219], v[176:179], v[42:45]
	v_mfma_f32_16x16x32_bf16 v[6:9], v[216:219], v[184:187], v[6:9]
	s_setprio 0
	s_barrier
	ds_read_b128 v[156:159], v148
	ds_read_b128 v[160:163], v149
	ds_read_b128 v[164:167], v150
	ds_read_b128 v[168:171], v151
	ds_read_b128 v[172:175], v152
	ds_read_b128 v[176:179], v153
	ds_read_b128 v[180:183], v154
	ds_read_b128 v[184:187], v155
	s_lshl_b32 s41, s41, 16
	s_or_b32 s42, s41, s28
	s_mov_b32 m0, s3
	s_lshl_b32 s42, s42, 1
	ds_read_b64_tr_b16 v[188:189], v146 offset:32768
	ds_read_b64_tr_b16 v[190:191], v146 offset:33280
	ds_read_b64_tr_b16 v[192:193], v147 offset:32768
	ds_read_b64_tr_b16 v[194:195], v147 offset:33280
	ds_read_b64_tr_b16 v[196:197], v146 offset:36864
	ds_read_b64_tr_b16 v[198:199], v146 offset:37376
	ds_read_b64_tr_b16 v[200:201], v147 offset:36864
	ds_read_b64_tr_b16 v[202:203], v147 offset:37376
	ds_read_b64_tr_b16 v[204:205], v222 offset:32768
	ds_read_b64_tr_b16 v[206:207], v222 offset:33280
	ds_read_b64_tr_b16 v[208:209], v223 offset:32768
	ds_read_b64_tr_b16 v[210:211], v223 offset:33280
	ds_read_b64_tr_b16 v[212:213], v222 offset:36864
	ds_read_b64_tr_b16 v[214:215], v222 offset:37376
	ds_read_b64_tr_b16 v[216:217], v223 offset:36864
	ds_read_b64_tr_b16 v[218:219], v223 offset:37376
	s_min_u32 s60, s37, 0x83
	s_add_i32 s60, s60, s16
	s_cmp_lt_u32 s60, 16
	s_cselect_b32 s61, s54, s55
	s_cselect_b32 s62, 0x20000, s63
	s_lshl_b32 s60, s60, 13
	s_add_i32 s56, s61, s60
	s_add_i32 s57, s56, s62
	s_add_i32 s58, s57, s62
	s_add_i32 s59, s58, s62
	buffer_load_dwordx4 v1, s[8:11], s56 offen lds
	s_mov_b32 m0, s27
	s_or_b32 s41, s41, s29
	buffer_load_dwordx4 v1, s[8:11], s57 offen lds
	s_lshl_b32 s41, s41, 1
	s_mov_b32 m0, s30
	s_nop 0
	buffer_load_dwordx4 v1, s[8:11], s58 offen lds
	s_mov_b32 m0, s31
	s_nop 0
	buffer_load_dwordx4 v1, s[8:11], s59 offen lds
	s_waitcnt lgkmcnt(15)
	s_barrier
	s_waitcnt lgkmcnt(0)
	s_setprio 1
	s_waitcnt lgkmcnt(7)
	v_mfma_f32_16x16x32_bf16 v[126:129], v[188:191], v[156:159], v[126:129]
	v_mfma_f32_16x16x32_bf16 v[94:97], v[188:191], v[164:167], v[94:97]
	s_waitcnt lgkmcnt(6)
	v_mfma_f32_16x16x32_bf16 v[122:125], v[192:195], v[156:159], v[122:125]
	v_mfma_f32_16x16x32_bf16 v[90:93], v[192:195], v[164:167], v[90:93]
	s_waitcnt lgkmcnt(3)
	v_mfma_f32_16x16x32_bf16 v[118:121], v[204:207], v[156:159], v[118:121]
	v_mfma_f32_16x16x32_bf16 v[86:89], v[204:207], v[164:167], v[86:89]
	s_waitcnt lgkmcnt(2)
	v_mfma_f32_16x16x32_bf16 v[114:117], v[208:211], v[156:159], v[114:117]
	v_mfma_f32_16x16x32_bf16 v[82:85], v[208:211], v[164:167], v[82:85]
	v_mfma_f32_16x16x32_bf16 v[126:129], v[196:199], v[160:163], v[126:129]
	v_mfma_f32_16x16x32_bf16 v[94:97], v[196:199], v[168:171], v[94:97]
	v_mfma_f32_16x16x32_bf16 v[122:125], v[200:203], v[160:163], v[122:125]
	v_mfma_f32_16x16x32_bf16 v[90:93], v[200:203], v[168:171], v[90:93]
	s_waitcnt lgkmcnt(1)
	v_mfma_f32_16x16x32_bf16 v[118:121], v[212:215], v[160:163], v[118:121]
	v_mfma_f32_16x16x32_bf16 v[86:89], v[212:215], v[168:171], v[86:89]
	s_waitcnt lgkmcnt(0)
	v_mfma_f32_16x16x32_bf16 v[114:117], v[216:219], v[160:163], v[114:117]
	v_mfma_f32_16x16x32_bf16 v[82:85], v[216:219], v[168:171], v[82:85]
	s_setprio 0
	s_setprio 1
	v_mfma_f32_16x16x32_bf16 v[62:65], v[188:191], v[172:175], v[62:65]
	v_mfma_f32_16x16x32_bf16 v[34:37], v[188:191], v[180:183], v[34:37]
	v_mfma_f32_16x16x32_bf16 v[58:61], v[192:195], v[172:175], v[58:61]
	v_mfma_f32_16x16x32_bf16 v[30:33], v[192:195], v[180:183], v[30:33]
	v_mfma_f32_16x16x32_bf16 v[54:57], v[204:207], v[172:175], v[54:57]
	v_mfma_f32_16x16x32_bf16 v[22:25], v[204:207], v[180:183], v[22:25]
	v_mfma_f32_16x16x32_bf16 v[50:53], v[208:211], v[172:175], v[50:53]
	v_mfma_f32_16x16x32_bf16 v[18:21], v[208:211], v[180:183], v[18:21]
	v_mfma_f32_16x16x32_bf16 v[62:65], v[196:199], v[176:179], v[62:65]
	v_mfma_f32_16x16x32_bf16 v[34:37], v[196:199], v[184:187], v[34:37]
	v_mfma_f32_16x16x32_bf16 v[58:61], v[200:203], v[176:179], v[58:61]
	v_mfma_f32_16x16x32_bf16 v[30:33], v[200:203], v[184:187], v[30:33]
	v_mfma_f32_16x16x32_bf16 v[54:57], v[212:215], v[176:179], v[54:57]
	v_mfma_f32_16x16x32_bf16 v[22:25], v[212:215], v[184:187], v[22:25]
	v_mfma_f32_16x16x32_bf16 v[50:53], v[216:219], v[176:179], v[50:53]
	v_mfma_f32_16x16x32_bf16 v[18:21], v[216:219], v[184:187], v[18:21]
	s_setprio 0
	s_barrier
	s_min_u32 s41, s40, 0x80
	s_lshl_b32 s41, s41, 18
	s_add_i32 s41, s41, 0xc0000
	s_or_b32 s42, s41, s23
	s_mov_b32 m0, s33
	s_lshl_b32 s42, s42, 1
	ds_read_b64_tr_b16 v[188:189], v146 offset:49152
	ds_read_b64_tr_b16 v[190:191], v146 offset:49664
	ds_read_b64_tr_b16 v[192:193], v147 offset:49152
	ds_read_b64_tr_b16 v[194:195], v147 offset:49664
	ds_read_b64_tr_b16 v[196:197], v146 offset:53248
	ds_read_b64_tr_b16 v[198:199], v146 offset:53760
	ds_read_b64_tr_b16 v[200:201], v147 offset:53248
	ds_read_b64_tr_b16 v[202:203], v147 offset:53760
	ds_read_b64_tr_b16 v[204:205], v222 offset:49152
	ds_read_b64_tr_b16 v[206:207], v222 offset:49664
	ds_read_b64_tr_b16 v[208:209], v223 offset:49152
	ds_read_b64_tr_b16 v[210:211], v223 offset:49664
	ds_read_b64_tr_b16 v[212:213], v222 offset:53248
	ds_read_b64_tr_b16 v[214:215], v222 offset:53760
	ds_read_b64_tr_b16 v[216:217], v223 offset:53248
	ds_read_b64_tr_b16 v[218:219], v223 offset:53760
	buffer_load_dwordx4 v130, s[4:7], s42 offen lds
	s_mov_b32 m0, s34
	s_or_b32 s41, s41, s24
	buffer_load_dwordx4 v133, s[4:7], s42 offen lds
	s_lshl_b32 s41, s41, 1
	s_mov_b32 m0, s35
	s_nop 0
	buffer_load_dwordx4 v130, s[4:7], s41 offen lds
	s_mov_b32 m0, s36
	s_nop 0
	buffer_load_dwordx4 v133, s[4:7], s41 offen lds
	s_waitcnt lgkmcnt(0)
	s_waitcnt vmcnt(4)
	s_barrier
	s_setprio 1
	s_waitcnt lgkmcnt(7)
	v_mfma_f32_16x16x32_bf16 v[110:113], v[188:191], v[156:159], v[110:113]
	v_mfma_f32_16x16x32_bf16 v[78:81], v[188:191], v[164:167], v[78:81]
	s_waitcnt lgkmcnt(6)
	v_mfma_f32_16x16x32_bf16 v[106:109], v[192:195], v[156:159], v[106:109]
	v_mfma_f32_16x16x32_bf16 v[74:77], v[192:195], v[164:167], v[74:77]
	s_waitcnt lgkmcnt(3)
	v_mfma_f32_16x16x32_bf16 v[102:105], v[204:207], v[156:159], v[102:105]
	v_mfma_f32_16x16x32_bf16 v[70:73], v[204:207], v[164:167], v[70:73]
	s_waitcnt lgkmcnt(2)
	v_mfma_f32_16x16x32_bf16 v[98:101], v[208:211], v[156:159], v[98:101]
	v_mfma_f32_16x16x32_bf16 v[66:69], v[208:211], v[164:167], v[66:69]
	v_mfma_f32_16x16x32_bf16 v[110:113], v[196:199], v[160:163], v[110:113]
	v_mfma_f32_16x16x32_bf16 v[78:81], v[196:199], v[168:171], v[78:81]
	v_mfma_f32_16x16x32_bf16 v[106:109], v[200:203], v[160:163], v[106:109]
	v_mfma_f32_16x16x32_bf16 v[74:77], v[200:203], v[168:171], v[74:77]
	s_waitcnt lgkmcnt(1)
	v_mfma_f32_16x16x32_bf16 v[102:105], v[212:215], v[160:163], v[102:105]
	v_mfma_f32_16x16x32_bf16 v[70:73], v[212:215], v[168:171], v[70:73]
	s_waitcnt lgkmcnt(0)
	v_mfma_f32_16x16x32_bf16 v[98:101], v[216:219], v[160:163], v[98:101]
	v_mfma_f32_16x16x32_bf16 v[66:69], v[216:219], v[168:171], v[66:69]
	s_setprio 0
	s_setprio 1
	v_mfma_f32_16x16x32_bf16 v[46:49], v[188:191], v[172:175], v[46:49]
	v_mfma_f32_16x16x32_bf16 v[10:13], v[188:191], v[180:183], v[10:13]
	v_mfma_f32_16x16x32_bf16 v[38:41], v[192:195], v[172:175], v[38:41]
	v_mfma_f32_16x16x32_bf16 v[2:5], v[192:195], v[180:183], v[2:5]
	v_mfma_f32_16x16x32_bf16 v[26:29], v[204:207], v[172:175], v[26:29]
	v_mfma_f32_16x16x32_bf16 v[14:17], v[204:207], v[180:183], v[14:17]
	v_mfma_f32_16x16x32_bf16 v[42:45], v[208:211], v[172:175], v[42:45]
	v_mfma_f32_16x16x32_bf16 v[6:9], v[208:211], v[180:183], v[6:9]
	v_mfma_f32_16x16x32_bf16 v[46:49], v[196:199], v[176:179], v[46:49]
	v_mfma_f32_16x16x32_bf16 v[10:13], v[196:199], v[184:187], v[10:13]
	v_mfma_f32_16x16x32_bf16 v[38:41], v[200:203], v[176:179], v[38:41]
	v_mfma_f32_16x16x32_bf16 v[2:5], v[200:203], v[184:187], v[2:5]
	v_mfma_f32_16x16x32_bf16 v[26:29], v[212:215], v[176:179], v[26:29]
	v_mfma_f32_16x16x32_bf16 v[14:17], v[212:215], v[184:187], v[14:17]
	v_mfma_f32_16x16x32_bf16 v[42:45], v[216:219], v[176:179], v[42:45]
	v_mfma_f32_16x16x32_bf16 v[6:9], v[216:219], v[184:187], v[6:9]
	s_setprio 0
	s_barrier
	s_add_i32 s41, s16, s37
	s_add_i32 s44, s41, -2
	s_cmpk_lt_u32 s40, 0x82
	s_cselect_b64 s[42:43], -1, 0
	s_cmp_gt_i32 s44, 13
	s_cselect_b64 s[44:45], -1, 0
	s_and_b64 s[42:43], s[42:43], s[44:45]
	s_andn2_b64 vcc, exec, s[42:43]
	s_cbranch_vccnz .LBB4_14
	s_add_i32 s41, s41, -16
	s_and_b32 s41, s41, 62
	s_cmp_lg_u32 s41, 0
	s_cbranch_scc1 .LBB4_14
	ds_read2_b32 v[156:157], v137 offset1:16
	ds_read2_b32 v[158:159], v137 offset0:128 offset1:144
	s_waitcnt lgkmcnt(1)
	v_pk_mul_f32 v[128:129], v[156:157], v[128:129] op_sel_hi:[0,1]
	v_pk_mul_f32 v[126:127], v[156:157], v[126:127] op_sel_hi:[0,1]
	v_pk_mul_f32 v[124:125], v[156:157], v[124:125] op_sel_hi:[0,1]
	v_pk_mul_f32 v[122:123], v[156:157], v[122:123] op_sel_hi:[0,1]
	v_pk_mul_f32 v[120:121], v[156:157], v[120:121] op_sel_hi:[0,1]
	v_pk_mul_f32 v[118:119], v[156:157], v[118:119] op_sel_hi:[0,1]
	v_pk_mul_f32 v[116:117], v[156:157], v[116:117] op_sel_hi:[0,1]
	v_pk_mul_f32 v[114:115], v[156:157], v[114:115] op_sel_hi:[0,1]
	v_pk_mul_f32 v[112:113], v[156:157], v[112:113] op_sel_hi:[0,1]
	v_pk_mul_f32 v[110:111], v[156:157], v[110:111] op_sel_hi:[0,1]
	v_pk_mul_f32 v[108:109], v[156:157], v[108:109] op_sel_hi:[0,1]
	v_pk_mul_f32 v[106:107], v[156:157], v[106:107] op_sel_hi:[0,1]
	v_pk_mul_f32 v[104:105], v[156:157], v[104:105] op_sel_hi:[0,1]
	v_pk_mul_f32 v[102:103], v[156:157], v[102:103] op_sel_hi:[0,1]
	v_pk_mul_f32 v[100:101], v[156:157], v[100:101] op_sel_hi:[0,1]
	v_pk_mul_f32 v[98:99], v[156:157], v[98:99] op_sel_hi:[0,1]
	v_mov_b32_e32 v156, v157
	v_pk_mul_f32 v[96:97], v[156:157], v[96:97] op_sel_hi:[0,1]
	v_pk_mul_f32 v[94:95], v[156:157], v[94:95] op_sel_hi:[0,1]
	v_pk_mul_f32 v[92:93], v[156:157], v[92:93] op_sel_hi:[0,1]
	v_pk_mul_f32 v[90:91], v[156:157], v[90:91] op_sel_hi:[0,1]
	v_pk_mul_f32 v[88:89], v[156:157], v[88:89] op_sel_hi:[0,1]
	v_pk_mul_f32 v[86:87], v[156:157], v[86:87] op_sel_hi:[0,1]
	v_pk_mul_f32 v[84:85], v[156:157], v[84:85] op_sel_hi:[0,1]
	v_pk_mul_f32 v[82:83], v[156:157], v[82:83] op_sel_hi:[0,1]
	v_pk_mul_f32 v[80:81], v[156:157], v[80:81] op_sel_hi:[0,1]
	v_pk_mul_f32 v[78:79], v[156:157], v[78:79] op_sel_hi:[0,1]
	v_pk_mul_f32 v[76:77], v[156:157], v[76:77] op_sel_hi:[0,1]
	v_pk_mul_f32 v[74:75], v[156:157], v[74:75] op_sel_hi:[0,1]
	v_pk_mul_f32 v[72:73], v[156:157], v[72:73] op_sel_hi:[0,1]
	v_pk_mul_f32 v[70:71], v[156:157], v[70:71] op_sel_hi:[0,1]
	v_pk_mul_f32 v[68:69], v[156:157], v[68:69] op_sel_hi:[0,1]
	v_pk_mul_f32 v[66:67], v[156:157], v[66:67] op_sel_hi:[0,1]
	s_waitcnt lgkmcnt(0)
	v_mov_b32_e32 v156, v159
	v_pk_mul_f32 v[64:65], v[158:159], v[64:65] op_sel_hi:[0,1]
	v_pk_mul_f32 v[62:63], v[158:159], v[62:63] op_sel_hi:[0,1]
	v_pk_mul_f32 v[60:61], v[158:159], v[60:61] op_sel_hi:[0,1]
	v_pk_mul_f32 v[58:59], v[158:159], v[58:59] op_sel_hi:[0,1]
	v_pk_mul_f32 v[56:57], v[158:159], v[56:57] op_sel_hi:[0,1]
	v_pk_mul_f32 v[54:55], v[158:159], v[54:55] op_sel_hi:[0,1]
	v_pk_mul_f32 v[52:53], v[158:159], v[52:53] op_sel_hi:[0,1]
	v_pk_mul_f32 v[50:51], v[158:159], v[50:51] op_sel_hi:[0,1]
	v_pk_mul_f32 v[48:49], v[158:159], v[48:49] op_sel_hi:[0,1]
	v_pk_mul_f32 v[46:47], v[158:159], v[46:47] op_sel_hi:[0,1]
	v_pk_mul_f32 v[40:41], v[158:159], v[40:41] op_sel_hi:[0,1]
	v_pk_mul_f32 v[38:39], v[158:159], v[38:39] op_sel_hi:[0,1]
	v_pk_mul_f32 v[28:29], v[158:159], v[28:29] op_sel_hi:[0,1]
	v_pk_mul_f32 v[26:27], v[158:159], v[26:27] op_sel_hi:[0,1]
	v_pk_mul_f32 v[44:45], v[158:159], v[44:45] op_sel_hi:[0,1]
	v_pk_mul_f32 v[42:43], v[158:159], v[42:43] op_sel_hi:[0,1]
	v_pk_mul_f32 v[36:37], v[156:157], v[36:37] op_sel_hi:[0,1]
	v_pk_mul_f32 v[34:35], v[156:157], v[34:35] op_sel_hi:[0,1]
	v_pk_mul_f32 v[32:33], v[156:157], v[32:33] op_sel_hi:[0,1]
	v_pk_mul_f32 v[30:31], v[156:157], v[30:31] op_sel_hi:[0,1]
	v_pk_mul_f32 v[24:25], v[156:157], v[24:25] op_sel_hi:[0,1]
	v_pk_mul_f32 v[22:23], v[156:157], v[22:23] op_sel_hi:[0,1]
	v_pk_mul_f32 v[20:21], v[156:157], v[20:21] op_sel_hi:[0,1]
	v_pk_mul_f32 v[18:19], v[156:157], v[18:19] op_sel_hi:[0,1]
	v_pk_mul_f32 v[12:13], v[156:157], v[12:13] op_sel_hi:[0,1]
	v_pk_mul_f32 v[10:11], v[156:157], v[10:11] op_sel_hi:[0,1]
	v_pk_mul_f32 v[4:5], v[156:157], v[4:5] op_sel_hi:[0,1]
	v_pk_mul_f32 v[2:3], v[156:157], v[2:3] op_sel_hi:[0,1]
	v_pk_mul_f32 v[16:17], v[156:157], v[16:17] op_sel_hi:[0,1]
	v_pk_mul_f32 v[14:15], v[156:157], v[14:15] op_sel_hi:[0,1]
	v_pk_mul_f32 v[8:9], v[156:157], v[8:9] op_sel_hi:[0,1]
	v_pk_mul_f32 v[6:7], v[156:157], v[6:7] op_sel_hi:[0,1]
	s_branch .LBB4_14

.LBB4_20:
	s_or_b64 exec, exec, s[2:3]
	v_lshlrev_b32_e32 v1, 5, v136
	v_or3_b32 v133, v1, v135, s13
	v_lshlrev_b32_e32 v1, 7, v136
	v_lshlrev_b32_e32 v130, 2, v135
	v_add3_u32 v1, s20, v1, v130
	v_add_u32_e32 v137, 0x800, v1
	v_lshlrev_b32_e32 v131, 2, v134
	ds_read2_b32 v[134:135], v137 offset1:16
	s_ashr_i32 s13, s12, 31
	s_lshl_b64 s[0:1], s[12:13], 23
	v_and_b32_e32 v130, 16, v0
	s_add_u32 s0, s14, s0
	s_waitcnt lgkmcnt(0)
	v_mul_f32_e32 v134, 0x3cb17218, v134
	v_pk_mul_f32 v[104:105], v[134:135], v[104:105] op_sel_hi:[0,1]
	v_pk_mul_f32 v[102:103], v[134:135], v[102:103] op_sel_hi:[0,1]
	v_pk_mul_f32 v[98:99], v[134:135], v[98:99] op_sel_hi:[0,1]
	v_cvt_pk_f16_f32 v102, v102, v103
	v_cvt_pk_f16_f32 v103, v104, v105
	v_cvt_pk_f16_f32 v104, v98, v99
	v_mul_f32_e32 v98, 0x3cb17218, v135
	v_pk_mul_f32 v[72:73], v[98:99], v[72:73] op_sel_hi:[0,1]
	v_pk_mul_f32 v[70:71], v[98:99], v[70:71] op_sel_hi:[0,1]
	v_pk_mul_f32 v[66:67], v[98:99], v[66:67] op_sel_hi:[0,1]
	v_cvt_pk_f16_f32 v70, v70, v71
	v_cvt_pk_f16_f32 v71, v72, v73
	v_cvt_pk_f16_f32 v72, v66, v67
	ds_read2_b32 v[66:67], v137 offset0:128 offset1:144
	v_lshlrev_b32_e32 v0, 6, v0
	v_and_or_b32 v136, v131, 8, v130
	s_addc_u32 s1, s15, s1
	v_and_b32_e32 v0, 64, v0
	v_mov_b32_e32 v1, 0
	v_lshl_add_u64 v[130:131], s[0:1], 0, v[0:1]
	v_lshlrev_b32_e32 v0, 1, v136
	v_lshl_add_u64 v[130:131], v[130:131], 0, v[0:1]
	v_lshlrev_b32_e32 v0, 11, v133
	v_and_b32_e32 v0, 0x7b7000, v0
	s_waitcnt lgkmcnt(0)
	v_mul_f32_e32 v66, 0x3cb17218, v66
	v_lshl_add_u64 v[130:131], v[130:131], 0, v[0:1]
	v_pk_mul_f32 v[100:101], v[134:135], v[100:101] op_sel_hi:[0,1]
	s_mov_b64 s[0:1], 0x8000
	v_pk_mul_f32 v[48:49], v[66:67], v[48:49] op_sel_hi:[0,1]
	v_pk_mul_f32 v[46:47], v[66:67], v[46:47] op_sel_hi:[0,1]
	v_pk_mul_f32 v[38:39], v[66:67], v[38:39] op_sel_hi:[0,1]
	v_pk_mul_f32 v[28:29], v[66:67], v[28:29] op_sel_hi:[0,1]
	v_pk_mul_f32 v[26:27], v[66:67], v[26:27] op_sel_hi:[0,1]
	v_lshlrev_b32_e32 v0, 8, v132
	v_cvt_pk_f16_f32 v105, v100, v101
	v_lshl_add_u64 v[100:101], v[130:131], 0, s[0:1]
	v_pk_mul_f32 v[68:69], v[98:99], v[68:69] op_sel_hi:[0,1]
	s_mov_b64 s[0:1], 0x40000
	v_cvt_pk_f16_f32 v46, v46, v47
	v_cvt_pk_f16_f32 v47, v48, v49
	v_cvt_pk_f16_f32 v48, v38, v39
	v_cvt_pk_f16_f32 v26, v26, v27
	v_cvt_pk_f16_f32 v27, v28, v29
	v_pk_mul_f32 v[38:39], v[66:67], v[44:45] op_sel_hi:[0,1]
	v_pk_mul_f32 v[28:29], v[66:67], v[42:43] op_sel_hi:[0,1]
	v_lshl_or_b32 v0, s21, 2, v0
	v_cvt_pk_f16_f32 v73, v68, v69
	v_lshl_add_u64 v[68:69], v[130:131], 0, s[0:1]
	v_pk_mul_f32 v[64:65], v[66:67], v[64:65] op_sel_hi:[0,1]
	v_pk_mul_f32 v[62:63], v[66:67], v[62:63] op_sel_hi:[0,1]
	v_pk_mul_f32 v[58:59], v[66:67], v[58:59] op_sel_hi:[0,1]
	v_cvt_pk_f16_f32 v28, v28, v29
	v_cvt_pk_f16_f32 v29, v38, v39
	v_cvt_pk_f16_f32 v62, v62, v63
	v_cvt_pk_f16_f32 v63, v64, v65
	v_cvt_pk_f16_f32 v64, v58, v59
	v_lshl_add_u64 v[58:59], v[68:69], 0, v[0:1]
	v_pk_mul_f32 v[40:41], v[66:67], v[40:41] op_sel_hi:[0,1]
	v_permlane16_swap_b32_e32 v26, v28
	v_permlane16_swap_b32_e32 v27, v29
	v_mul_f32_e32 v38, 0x3cb17218, v67
	s_mov_b64 s[0:1], 0x48000
	v_pk_mul_f32 v[128:129], v[134:135], v[128:129] op_sel_hi:[0,1]
	v_pk_mul_f32 v[126:127], v[134:135], v[126:127] op_sel_hi:[0,1]
	v_pk_mul_f32 v[122:123], v[134:135], v[122:123] op_sel_hi:[0,1]
	v_pk_mul_f32 v[96:97], v[98:99], v[96:97] op_sel_hi:[0,1]
	v_pk_mul_f32 v[94:95], v[98:99], v[94:95] op_sel_hi:[0,1]
	v_pk_mul_f32 v[90:91], v[98:99], v[90:91] op_sel_hi:[0,1]
	v_pk_mul_f32 v[88:89], v[98:99], v[88:89] op_sel_hi:[0,1]
	v_pk_mul_f32 v[86:87], v[98:99], v[86:87] op_sel_hi:[0,1]
	v_pk_mul_f32 v[82:83], v[98:99], v[82:83] op_sel_hi:[0,1]
	v_cvt_pk_f16_f32 v49, v40, v41
	global_store_dwordx4 v[58:59], v[26:29], off offset:640
	v_lshl_add_u64 v[40:41], v[130:131], 0, s[0:1]
	v_cvt_pk_f16_f32 v126, v126, v127
	v_pk_mul_f32 v[28:29], v[38:39], v[36:37] op_sel_hi:[0,1]
	v_pk_mul_f32 v[26:27], v[38:39], v[34:35] op_sel_hi:[0,1]
	v_cvt_pk_f16_f32 v127, v128, v129
	v_cvt_pk_f16_f32 v128, v122, v123
	v_lshl_add_u64 v[122:123], v[130:131], 0, v[0:1]
	v_cvt_pk_f16_f32 v94, v94, v95
	v_cvt_pk_f16_f32 v95, v96, v97
	v_cvt_pk_f16_f32 v96, v90, v91
	v_lshl_add_u64 v[90:91], v[100:101], 0, v[0:1]
	v_cvt_pk_f16_f32 v86, v86, v87
	v_cvt_pk_f16_f32 v87, v88, v89
	v_cvt_pk_f16_f32 v88, v82, v83
	v_or_b32_e32 v82, 0x80, v0
	v_mov_b32_e32 v83, v1
	v_cvt_pk_f16_f32 v26, v26, v27
	v_cvt_pk_f16_f32 v27, v28, v29
	v_pk_mul_f32 v[28:29], v[38:39], v[30:31] op_sel_hi:[0,1]
	v_lshl_add_u64 v[30:31], v[40:41], 0, v[0:1]
	v_pk_mul_f32 v[0:1], v[38:39], v[24:25] op_sel_hi:[0,1]
	v_pk_mul_f32 v[22:23], v[38:39], v[22:23] op_sel_hi:[0,1]
	v_cvt_pk_f16_f32 v22, v22, v23
	v_cvt_pk_f16_f32 v23, v0, v1
	v_pk_mul_f32 v[0:1], v[38:39], v[20:21] op_sel_hi:[0,1]
	v_pk_mul_f32 v[18:19], v[38:39], v[18:19] op_sel_hi:[0,1]
	v_cvt_pk_f16_f32 v24, v18, v19
	v_cvt_pk_f16_f32 v25, v0, v1
	s_nop 0
	v_permlane16_swap_b32_e32 v22, v24
	v_permlane16_swap_b32_e32 v23, v25
	v_lshl_add_u64 v[0:1], v[40:41], 0, v[82:83]
	global_store_dwordx4 v[0:1], v[22:25], off
	v_pk_mul_f32 v[12:13], v[38:39], v[12:13] op_sel_hi:[0,1]
	v_pk_mul_f32 v[0:1], v[38:39], v[10:11] op_sel_hi:[0,1]
	v_pk_mul_f32 v[4:5], v[38:39], v[4:5] op_sel_hi:[0,1]
	v_pk_mul_f32 v[2:3], v[38:39], v[2:3] op_sel_hi:[0,1]
	v_cvt_pk_f16_f32 v0, v0, v1
	v_cvt_pk_f16_f32 v1, v12, v13
	v_cvt_pk_f16_f32 v2, v2, v3
	v_cvt_pk_f16_f32 v3, v4, v5
	s_nop 0
	v_permlane16_swap_b32_e32 v0, v2
	v_permlane16_swap_b32_e32 v1, v3
	global_store_dwordx4 v[30:31], v[0:3], off offset:512
	v_pk_mul_f32 v[124:125], v[134:135], v[124:125] op_sel_hi:[0,1]
	v_pk_mul_f32 v[120:121], v[134:135], v[120:121] op_sel_hi:[0,1]
	v_pk_mul_f32 v[2:3], v[38:39], v[16:17] op_sel_hi:[0,1]
	v_pk_mul_f32 v[0:1], v[38:39], v[14:15] op_sel_hi:[0,1]
	v_pk_mul_f32 v[118:119], v[134:135], v[118:119] op_sel_hi:[0,1]
	v_pk_mul_f32 v[116:117], v[134:135], v[116:117] op_sel_hi:[0,1]
	v_pk_mul_f32 v[114:115], v[134:135], v[114:115] op_sel_hi:[0,1]
	v_pk_mul_f32 v[112:113], v[134:135], v[112:113] op_sel_hi:[0,1]
	v_pk_mul_f32 v[110:111], v[134:135], v[110:111] op_sel_hi:[0,1]
	v_pk_mul_f32 v[108:109], v[134:135], v[108:109] op_sel_hi:[0,1]
	v_pk_mul_f32 v[106:107], v[134:135], v[106:107] op_sel_hi:[0,1]
	v_pk_mul_f32 v[92:93], v[98:99], v[92:93] op_sel_hi:[0,1]
	v_pk_mul_f32 v[84:85], v[98:99], v[84:85] op_sel_hi:[0,1]
	v_pk_mul_f32 v[80:81], v[98:99], v[80:81] op_sel_hi:[0,1]
	v_pk_mul_f32 v[78:79], v[98:99], v[78:79] op_sel_hi:[0,1]
	v_pk_mul_f32 v[76:77], v[98:99], v[76:77] op_sel_hi:[0,1]
	v_pk_mul_f32 v[74:75], v[98:99], v[74:75] op_sel_hi:[0,1]
	v_pk_mul_f32 v[60:61], v[66:67], v[60:61] op_sel_hi:[0,1]
	v_pk_mul_f32 v[56:57], v[66:67], v[56:57] op_sel_hi:[0,1]
	v_pk_mul_f32 v[54:55], v[66:67], v[54:55] op_sel_hi:[0,1]
	v_pk_mul_f32 v[52:53], v[66:67], v[52:53] op_sel_hi:[0,1]
	v_pk_mul_f32 v[50:51], v[66:67], v[50:51] op_sel_hi:[0,1]
	v_pk_mul_f32 v[32:33], v[38:39], v[32:33] op_sel_hi:[0,1]
	v_cvt_pk_f16_f32 v0, v0, v1
	v_cvt_pk_f16_f32 v1, v2, v3
	v_pk_mul_f32 v[4:5], v[38:39], v[8:9] op_sel_hi:[0,1]
	v_pk_mul_f32 v[2:3], v[38:39], v[6:7] op_sel_hi:[0,1]
	v_cvt_pk_f16_f32 v129, v124, v125
	v_cvt_pk_f16_f32 v118, v118, v119
	v_cvt_pk_f16_f32 v119, v120, v121
	v_cvt_pk_f16_f32 v120, v114, v115
	v_cvt_pk_f16_f32 v121, v116, v117
	v_cvt_pk_f16_f32 v110, v110, v111
	v_cvt_pk_f16_f32 v111, v112, v113
	v_cvt_pk_f16_f32 v112, v106, v107
	v_cvt_pk_f16_f32 v113, v108, v109
	v_cvt_pk_f16_f32 v97, v92, v93
	v_cvt_pk_f16_f32 v89, v84, v85
	v_cvt_pk_f16_f32 v78, v78, v79
	v_cvt_pk_f16_f32 v79, v80, v81
	v_cvt_pk_f16_f32 v80, v74, v75
	v_cvt_pk_f16_f32 v81, v76, v77
	v_cvt_pk_f16_f32 v65, v60, v61
	v_cvt_pk_f16_f32 v54, v54, v55
	v_cvt_pk_f16_f32 v55, v56, v57
	v_cvt_pk_f16_f32 v56, v50, v51
	v_cvt_pk_f16_f32 v57, v52, v53
	v_cvt_pk_f16_f32 v28, v28, v29
	v_cvt_pk_f16_f32 v29, v32, v33
	v_cvt_pk_f16_f32 v2, v2, v3
	v_cvt_pk_f16_f32 v3, v4, v5
	v_permlane16_swap_b32_e32 v126, v128
	v_permlane16_swap_b32_e32 v127, v129
	v_permlane16_swap_b32_e32 v118, v120
	v_permlane16_swap_b32_e32 v119, v121
	v_permlane16_swap_b32_e32 v110, v112
	v_permlane16_swap_b32_e32 v111, v113
	v_permlane16_swap_b32_e32 v102, v104
	v_permlane16_swap_b32_e32 v103, v105
	v_permlane16_swap_b32_e32 v94, v96
	v_permlane16_swap_b32_e32 v95, v97
	v_permlane16_swap_b32_e32 v86, v88
	v_permlane16_swap_b32_e32 v87, v89
	v_lshl_add_u64 v[84:85], v[100:101], 0, v[82:83]
	v_permlane16_swap_b32_e32 v78, v80
	v_permlane16_swap_b32_e32 v79, v81
	v_permlane16_swap_b32_e32 v70, v72
	v_permlane16_swap_b32_e32 v71, v73
	v_permlane16_swap_b32_e32 v62, v64
	v_permlane16_swap_b32_e32 v63, v65
	v_permlane16_swap_b32_e32 v54, v56
	v_permlane16_swap_b32_e32 v55, v57
	v_lshl_add_u64 v[50:51], v[68:69], 0, v[82:83]
	v_permlane16_swap_b32_e32 v46, v48
	v_permlane16_swap_b32_e32 v47, v49
	v_permlane16_swap_b32_e32 v26, v28
	v_permlane16_swap_b32_e32 v27, v29
	v_permlane16_swap_b32_e32 v0, v2
	v_permlane16_swap_b32_e32 v1, v3
	global_store_dwordx4 v[122:123], v[126:129], off
	global_store_dwordx4 v[122:123], v[118:121], off offset:128
	global_store_dwordx4 v[122:123], v[110:113], off offset:512
	global_store_dwordx4 v[122:123], v[102:105], off offset:640
	global_store_dwordx4 v[90:91], v[94:97], off
	global_store_dwordx4 v[84:85], v[86:89], off
	global_store_dwordx4 v[90:91], v[78:81], off offset:512
	global_store_dwordx4 v[90:91], v[70:73], off offset:640
	global_store_dwordx4 v[58:59], v[62:65], off
	global_store_dwordx4 v[50:51], v[54:57], off
	global_store_dwordx4 v[58:59], v[46:49], off offset:512
	global_store_dwordx4 v[30:31], v[26:29], off
	global_store_dwordx4 v[30:31], v[0:3], off offset:640
	s_endpgm
	.p2alignl 8, 3212836864

	.amdhsa_kernel _Z6gemm_kILi2EEvPKDF16_S1_iiiiPfPDF16_PKfS2_
		.amdhsa_group_segment_fixed_size 0
		.amdhsa_private_segment_fixed_size 0
		.amdhsa_kernarg_size 64
		.amdhsa_user_sgpr_count 2
		.amdhsa_user_sgpr_dispatch_ptr 0
		.amdhsa_user_sgpr_queue_ptr 0
		.amdhsa_user_sgpr_kernarg_segment_ptr 1
		.amdhsa_user_sgpr_dispatch_id 0
		.amdhsa_user_sgpr_kernarg_preload_length 0
		.amdhsa_user_sgpr_kernarg_preload_offset 0
		.amdhsa_user_sgpr_private_segment_size 0
		.amdhsa_uses_dynamic_stack 0
		.amdhsa_enable_private_segment 0
		.amdhsa_system_sgpr_workgroup_id_x 1
		.amdhsa_system_sgpr_workgroup_id_y 0
		.amdhsa_system_sgpr_workgroup_id_z 0
		.amdhsa_system_sgpr_workgroup_info 0
		.amdhsa_system_vgpr_workitem_id 0
		.amdhsa_next_free_vgpr 224
		.amdhsa_next_free_sgpr 64
		.amdhsa_accum_offset 224
		.amdhsa_reserve_vcc 1
		.amdhsa_float_round_mode_32 0
		.amdhsa_float_round_mode_16_64 0
		.amdhsa_float_denorm_mode_32 3
		.amdhsa_float_denorm_mode_16_64 3
		.amdhsa_dx10_clamp 1
		.amdhsa_ieee_mode 1
		.amdhsa_fp16_overflow 0
		.amdhsa_tg_split 0
		.amdhsa_exception_fp_ieee_invalid_op 0
		.amdhsa_exception_fp_denorm_src 0
		.amdhsa_exception_fp_ieee_div_zero 0
		.amdhsa_exception_fp_ieee_overflow 0
		.amdhsa_exception_fp_ieee_underflow 0
		.amdhsa_exception_fp_ieee_inexact 0
		.amdhsa_exception_int_div_zero 0
	.end_amdhsa_kernel

amdhsa.kernels:
  - .agpr_count:     0
    .args:
      - .actual_access:  read_only
        .address_space:  global
        .offset:         0
        .size:           8
        .value_kind:     global_buffer
      - .actual_access:  read_only
        .address_space:  global
        .offset:         8
        .size:           8
        .value_kind:     global_buffer
      - .actual_access:  read_only
        .address_space:  global
        .offset:         16
        .size:           8
        .value_kind:     global_buffer
      - .actual_access:  write_only
        .address_space:  global
        .offset:         24
        .size:           8
        .value_kind:     global_buffer
      - .actual_access:  write_only
        .address_space:  global
        .offset:         32
        .size:           8
        .value_kind:     global_buffer
      - .actual_access:  write_only
        .address_space:  global
        .offset:         40
        .size:           8
        .value_kind:     global_buffer
      - .actual_access:  write_only
        .address_space:  global
        .offset:         48
        .size:           8
        .value_kind:     global_buffer
      - .actual_access:  read_only
        .address_space:  global
        .offset:         56
        .size:           8
        .value_kind:     global_buffer
      - .actual_access:  read_only
        .address_space:  global
        .offset:         64
        .size:           8
        .value_kind:     global_buffer
      - .actual_access:  write_only
        .address_space:  global
        .offset:         72
        .size:           8
        .value_kind:     global_buffer
    .group_segment_fixed_size: 8448
    .kernarg_segment_align: 8
    .kernarg_segment_size: 80
    .language:       OpenCL C
    .language_version:
      - 2
      - 0
    .max_flat_workgroup_size: 256
    .name:           _Z6prep_kPKfS0_S0_PDF16_S1_S1_S1_S1_S0_Pf
    .private_segment_fixed_size: 0
    .sgpr_count:     22
    .sgpr_spill_count: 0
    .symbol:         _Z6prep_kPKfS0_S0_PDF16_S1_S1_S1_S1_S0_Pf.kd
    .uniform_work_group_size: 1
    .uses_dynamic_stack: false
    .vgpr_count:     34
    .vgpr_spill_count: 0
    .wavefront_size: 64
  - .agpr_count:     0
    .args:
      - .actual_access:  read_only
        .address_space:  global
        .offset:         0
        .size:           8
        .value_kind:     global_buffer
      - .actual_access:  write_only
        .address_space:  global
        .offset:         8
        .size:           8
        .value_kind:     global_buffer
      - .actual_access:  read_only
        .address_space:  global
        .offset:         16
        .size:           8
        .value_kind:     global_buffer
      - .actual_access:  write_only
        .address_space:  global
        .offset:         24
        .size:           8
        .value_kind:     global_buffer
      - .offset:         32
        .size:           4
        .value_kind:     hidden_block_count_x
      - .offset:         36
        .size:           4
        .value_kind:     hidden_block_count_y
      - .offset:         40
        .size:           4
        .value_kind:     hidden_block_count_z
      - .offset:         44
        .size:           2
        .value_kind:     hidden_group_size_x
      - .offset:         46
        .size:           2
        .value_kind:     hidden_group_size_y
      - .offset:         48
        .size:           2
        .value_kind:     hidden_group_size_z
      - .offset:         50
        .size:           2
        .value_kind:     hidden_remainder_x
      - .offset:         52
        .size:           2
        .value_kind:     hidden_remainder_y
      - .offset:         54
        .size:           2
        .value_kind:     hidden_remainder_z
      - .offset:         72
        .size:           8
        .value_kind:     hidden_global_offset_x
      - .offset:         80
        .size:           8
        .value_kind:     hidden_global_offset_y
      - .offset:         88
        .size:           8
        .value_kind:     hidden_global_offset_z
      - .offset:         96
        .size:           2
        .value_kind:     hidden_grid_dims
    .group_segment_fixed_size: 0
    .kernarg_segment_align: 8
    .kernarg_segment_size: 288
    .language:       OpenCL C
    .language_version:
      - 2
      - 0
    .max_flat_workgroup_size: 1024
    .name:           _Z6post_kPKfPfPKDF16_PDF16_
    .private_segment_fixed_size: 0
    .sgpr_count:     14
    .sgpr_spill_count: 0
    .symbol:         _Z6post_kPKfPfPKDF16_PDF16_.kd
    .uniform_work_group_size: 1
    .uses_dynamic_stack: false
    .vgpr_count:     49
    .vgpr_spill_count: 0
    .wavefront_size: 64
  - .agpr_count:     0
    .args:
      - .actual_access:  read_only
        .address_space:  global
        .offset:         0
        .size:           8
        .value_kind:     global_buffer
      - .actual_access:  read_only
        .address_space:  global
        .offset:         8
        .size:           8
        .value_kind:     global_buffer
      - .actual_access:  write_only
        .address_space:  global
        .offset:         16
        .size:           8
        .value_kind:     global_buffer
      - .offset:         24
        .size:           4
        .value_kind:     hidden_block_count_x
      - .offset:         28
        .size:           4
        .value_kind:     hidden_block_count_y
      - .offset:         32
        .size:           4
        .value_kind:     hidden_block_count_z
      - .offset:         36
        .size:           2
        .value_kind:     hidden_group_size_x
      - .offset:         38
        .size:           2
        .value_kind:     hidden_group_size_y
      - .offset:         40
        .size:           2
        .value_kind:     hidden_group_size_z
      - .offset:         42
        .size:           2
        .value_kind:     hidden_remainder_x
      - .offset:         44
        .size:           2
        .value_kind:     hidden_remainder_y
      - .offset:         46
        .size:           2
        .value_kind:     hidden_remainder_z
      - .offset:         64
        .size:           8
        .value_kind:     hidden_global_offset_x
      - .offset:         72
        .size:           8
        .value_kind:     hidden_global_offset_y
      - .offset:         80
        .size:           8
        .value_kind:     hidden_global_offset_z
      - .offset:         88
        .size:           2
        .value_kind:     hidden_grid_dims
    .group_segment_fixed_size: 0
    .kernarg_segment_align: 8
    .kernarg_segment_size: 280
    .language:       OpenCL C
    .language_version:
      - 2
      - 0
    .max_flat_workgroup_size: 1024
    .name:           _Z8reduce_kPKDF16_PKfPf
    .private_segment_fixed_size: 0
    .sgpr_count:     16
    .sgpr_spill_count: 0
    .symbol:         _Z8reduce_kPKDF16_PKfPf.kd
    .uniform_work_group_size: 1
    .uses_dynamic_stack: false
    .vgpr_count:     42
    .vgpr_spill_count: 0
    .wavefront_size: 64
  - .agpr_count:     0
    .args:
      - .actual_access:  read_only
        .address_space:  global
        .offset:         0
        .size:           8
        .value_kind:     global_buffer
      - .actual_access:  read_only
        .address_space:  global
        .offset:         8
        .size:           8
        .value_kind:     global_buffer
      - .actual_access:  write_only
        .address_space:  global
        .offset:         16
        .size:           8
        .value_kind:     global_buffer
      - .address_space:  global
        .offset:         24
        .size:           8
        .value_kind:     global_buffer
      - .actual_access:  write_only
        .address_space:  global
        .offset:         32
        .size:           8
        .value_kind:     global_buffer
      - .actual_access:  read_only
        .address_space:  global
        .offset:         40
        .size:           8
        .value_kind:     global_buffer
      - .actual_access:  write_only
        .address_space:  global
        .offset:         48
        .size:           8
        .value_kind:     global_buffer
    .group_segment_fixed_size: 0
    .kernarg_segment_align: 8
    .kernarg_segment_size: 56
    .language:       OpenCL C
    .language_version:
      - 2
      - 0
    .max_flat_workgroup_size: 512
    .name:           _Z7gemm1_kPKDF16_S0_PDF16_PKfPfS0_S1_
    .private_segment_fixed_size: 0
    .sgpr_count:     72
    .sgpr_spill_count: 0
    .symbol:         _Z7gemm1_kPKDF16_S0_PDF16_PKfPfS0_S1_.kd
    .uniform_work_group_size: 1
    .uses_dynamic_stack: false
    .vgpr_count:     232
    .vgpr_spill_count: 0
    .wavefront_size: 64
  - .agpr_count:     0
    .args:
      - .actual_access:  read_only
        .address_space:  global
        .offset:         0
        .size:           8
        .value_kind:     global_buffer
      - .actual_access:  read_only
        .address_space:  global
        .offset:         8
        .size:           8
        .value_kind:     global_buffer
      - .offset:         16
        .size:           4
        .value_kind:     by_value
      - .offset:         20
        .size:           4
        .value_kind:     by_value
      - .offset:         24
        .size:           4
        .value_kind:     by_value
      - .offset:         28
        .size:           4
        .value_kind:     by_value
      - .actual_access:  read_only
        .address_space:  global
        .offset:         32
        .size:           8
        .value_kind:     global_buffer
      - .actual_access:  write_only
        .address_space:  global
        .offset:         40
        .size:           8
        .value_kind:     global_buffer
      - .actual_access:  read_only
        .address_space:  global
        .offset:         48
        .size:           8
        .value_kind:     global_buffer
      - .actual_access:  read_only
        .address_space:  global
        .offset:         56
        .size:           8
        .value_kind:     global_buffer
    .group_segment_fixed_size: 0
    .kernarg_segment_align: 8
    .kernarg_segment_size: 64
    .language:       OpenCL C
    .language_version:
      - 2
      - 0
    .max_flat_workgroup_size: 512
    .name:           _Z6gemm_kILi2EEvPKDF16_S1_iiiiPfPDF16_PKfS2_
    .private_segment_fixed_size: 0
    .sgpr_count:     70
    .sgpr_spill_count: 0
    .symbol:         _Z6gemm_kILi2EEvPKDF16_S1_iiiiPfPDF16_PKfS2_.kd
    .uniform_work_group_size: 1
    .uses_dynamic_stack: false
    .vgpr_count:     224
    .vgpr_spill_count: 0
    .wavefront_size: 64
  - .agpr_count:     0
    .args:
      - .actual_access:  read_only
        .address_space:  global
        .offset:         0
        .size:           8
        .value_kind:     global_buffer
      - .actual_access:  read_only
        .address_space:  global
        .offset:         8
        .size:           8
        .value_kind:     global_buffer
      - .offset:         16
        .size:           4
        .value_kind:     by_value
      - .offset:         20
        .size:           4
        .value_kind:     by_value
      - .offset:         24
        .size:           4
        .value_kind:     by_value
      - .offset:         28
        .size:           4
        .value_kind:     by_value
      - .actual_access:  read_only
        .address_space:  global
        .offset:         32
        .size:           8
        .value_kind:     global_buffer
      - .actual_access:  write_only
        .address_space:  global
        .offset:         40
        .size:           8
        .value_kind:     global_buffer
      - .actual_access:  read_only
        .address_space:  global
        .offset:         48
        .size:           8
        .value_kind:     global_buffer
      - .actual_access:  read_only
        .address_space:  global
        .offset:         56
        .size:           8
        .value_kind:     global_buffer
    .group_segment_fixed_size: 0
    .kernarg_segment_align: 8
    .kernarg_segment_size: 64
    .language:       OpenCL C
    .language_version:
      - 2
      - 0
    .max_flat_workgroup_size: 512
    .name:           _Z6gemm_kILi3EEvPKDF16_S1_iiiiPfPDF16_PKfS2_
    .private_segment_fixed_size: 0
    .sgpr_count:     51
    .sgpr_spill_count: 0
    .symbol:         _Z6gemm_kILi3EEvPKDF16_S1_iiiiPfPDF16_PKfS2_.kd
    .uniform_work_group_size: 1
    .uses_dynamic_stack: false
    .vgpr_count:     220
    .vgpr_spill_count: 0
    .wavefront_size: 64
